# speedup vs baseline: 1.0020x; 1.0012x over previous
_Z8gemm_qkvPKDF16_S0_PKfS2_S2_PDF16_S3_S3_:
	s_load_dwordx8 s[12:19], s[0:1], 0x0
	s_load_dwordx8 s[4:11], s[0:1], 0x20
	s_mov_b32 s66, s2
	s_bitcmp0_b32 s2, 7
	s_mov_b64 s[0:1], -1
	s_cbranch_scc0 .LBB1_3
	s_and_b64 vcc, exec, s[0:1]
	s_cbranch_vccnz .LBB1_60
